# MLA loop: reference-max held in the QK accumulator init (rare rebase when a row max exceeds it by >4), waves 4-7 staggered by half a tile, lazy rescale
# speedup vs baseline: 1.0604x; 1.0247x over previous
; __device__ __forceinline__ float xhalf_max(float v) { auto rr = __builtin_amdgcn_permlane32_swap(__float_as_uint(v), __float_as_uint(v), false, false); return fmaxf(__uint_as_float(rr[0]), __uint_as_float(rr[1])); }
; template <bool ALIBI>
; __device__ __forceinline__ void attn_sv(const LAS unsigned char* kb, int vfo, f32x16& p0, f32x16& p1, float& m, float& l, f32x16& o0, f32x16& o1, int hi, int tq, int kpos0, float slope2, bool causal) {
;     ...
;     float rm = fmaxf(p0[0], p1[0]);
; #pragma unroll
;     for (int r = 1; r < 16; ++r) rm = fmaxf(rm, fmaxf(p0[r], p1[r]));
;     rm = xhalf_max(rm);
;     const float mn = fmaxf(m, rm), alpha = __builtin_amdgcn_exp2f(m - mn);
.Lmla0_pre_nomask:
	v_max3_f32 v218, v2, v3, v4
	v_max3_f32 v219, v18, v19, v20
	v_max3_f32 v218, v218, v5, v6
	v_max3_f32 v219, v219, v21, v22
	v_max3_f32 v218, v218, v7, v8
	v_max3_f32 v219, v219, v23, v24
	v_max3_f32 v218, v218, v9, v10
	v_max3_f32 v219, v219, v25, v26
	v_max3_f32 v218, v218, v11, v12
	v_max3_f32 v219, v219, v27, v28
	v_max3_f32 v218, v218, v13, v14
	v_max3_f32 v219, v219, v29, v30
	v_max3_f32 v218, v218, v15, v16
	v_max3_f32 v219, v219, v31, v32
	v_max3_f32 v218, v218, v17, v219
	v_max_f32_e32 v218, v218, v33
	v_mov_b32_e32 v219, v218
	s_nop 1
	v_permlane32_swap_b32_e32 v218, v219
	v_max_f32_e32 v214, v218, v219
	s_nop 0
	v_sub_f32_e32 v222, 0, v214
	v_sub_f32_e32 v223, 0, v214
	v_sub_f32_e32 v224, 0, v214
	v_sub_f32_e32 v225, 0, v214
	v_sub_f32_e32 v226, 0, v214
	v_sub_f32_e32 v227, 0, v214
	v_sub_f32_e32 v228, 0, v214
	v_sub_f32_e32 v229, 0, v214
	v_sub_f32_e32 v230, 0, v214
	v_sub_f32_e32 v231, 0, v214
	v_sub_f32_e32 v232, 0, v214
	v_sub_f32_e32 v233, 0, v214
	v_sub_f32_e32 v234, 0, v214
	v_sub_f32_e32 v235, 0, v214
	v_sub_f32_e32 v236, 0, v214
	v_sub_f32_e32 v237, 0, v214
	v_sub_f32_e32 v18, v18, v214
	v_sub_f32_e32 v19, v19, v214
	v_sub_f32_e32 v20, v20, v214
	v_sub_f32_e32 v21, v21, v214
	v_sub_f32_e32 v22, v22, v214
	v_sub_f32_e32 v23, v23, v214
	v_sub_f32_e32 v24, v24, v214
	v_sub_f32_e32 v25, v25, v214
	v_sub_f32_e32 v26, v26, v214
	v_sub_f32_e32 v27, v27, v214
	v_sub_f32_e32 v28, v28, v214
	v_sub_f32_e32 v29, v29, v214
	v_sub_f32_e32 v30, v30, v214
	v_sub_f32_e32 v31, v31, v214
	v_sub_f32_e32 v32, v32, v214
	v_sub_f32_e32 v33, v33, v214
	v_sub_f32_e32 v2, v2, v214
	v_sub_f32_e32 v3, v3, v214
	v_sub_f32_e32 v4, v4, v214
	v_sub_f32_e32 v5, v5, v214
	v_sub_f32_e32 v6, v6, v214
	v_sub_f32_e32 v7, v7, v214
	v_sub_f32_e32 v8, v8, v214
	v_sub_f32_e32 v9, v9, v214
	v_sub_f32_e32 v10, v10, v214
	v_sub_f32_e32 v11, v11, v214
	v_sub_f32_e32 v12, v12, v214
	v_sub_f32_e32 v13, v13, v214
	v_sub_f32_e32 v14, v14, v214
	v_sub_f32_e32 v15, v15, v214
	v_sub_f32_e32 v16, v16, v214
	v_sub_f32_e32 v17, v17, v214
	s_mov_b64 s[90:91], 0

; #define LAS __attribute__((address_space(3)))
; template <int DQK>
; __device__ __forceinline__ void attn_qk(const LAS unsigned char* kb, int kfo, const bf16x8 (&qf)[DQK / 16], f32x16& p0, f32x16& p1) {
;     constexpr int ND0 = DQK / 16;
;     bf16x8 ka[ND0], kc[ND0];
; #pragma unroll
;     for (int d0 = 0; d0 < ND0; ++d0) { ka[d0] = *(const LAS bf16x8*)(kb + kfo + d0 * 2048); kc[d0] = *(const LAS bf16x8*)(kb + kfo + d0 * 2048 + 512); }
;     __builtin_amdgcn_sched_barrier(0);
; #pragma unroll
;     for (int r = 0; r < 16; ++r) { p0[r] = 0.f; p1[r] = 0.f; }
; #pragma unroll
;     for (int d0 = 0; d0 < ND0; ++d0) {
;         p0 = __builtin_amdgcn_mfma_f32_32x32x16_bf16(ka[d0], qf[d0], p0, 0, 0, 0);
;         p1 = __builtin_amdgcn_mfma_f32_32x32x16_bf16(kc[d0], qf[d0], p1, 0, 0, 0);
;     }
; template <bool ALIBI>
; __device__ __forceinline__ void attn_sv(const LAS unsigned char* kb, int vfo, f32x16& p0, f32x16& p1, float& m, float& l, f32x16& o0, f32x16& o1, int hi, int tq, int kpos0, float slope2, bool causal) {
;     ...
;     float ls = 0.f;
; #pragma unroll
;     for (int r = 0; r < 16; ++r) { p0[r] = __builtin_amdgcn_exp2f(p0[r] - mn); p1[r] = __builtin_amdgcn_exp2f(p1[r] - mn); ls += p0[r] + p1[r]; }
;     l = l * alpha + ls;
; #pragma unroll
;     for (int r = 0; r < 16; ++r) { o0[r] *= alpha; o1[r] *= alpha; }
.Lmla0_h0_noiss:
	s_cmp_lg_u64 s[90:91], 0
	s_cbranch_scc0 .Lmla0_h0_noresc
	v_max_f32_e32 v218, 0, v214
	v_exp_f32_e64 v186, -v218
	v_sub_f32_e32 v18, v18, v218
	v_sub_f32_e32 v19, v19, v218
	v_sub_f32_e32 v20, v20, v218
	v_sub_f32_e32 v21, v21, v218
	v_sub_f32_e32 v22, v22, v218
	v_sub_f32_e32 v23, v23, v218
	v_sub_f32_e32 v24, v24, v218
	v_sub_f32_e32 v25, v25, v218
	v_sub_f32_e32 v26, v26, v218
	v_sub_f32_e32 v27, v27, v218
	v_sub_f32_e32 v28, v28, v218
	v_sub_f32_e32 v29, v29, v218
	v_sub_f32_e32 v30, v30, v218
	v_sub_f32_e32 v31, v31, v218
	v_sub_f32_e32 v32, v32, v218
	v_sub_f32_e32 v33, v33, v218
	v_sub_f32_e32 v2, v2, v218
	v_sub_f32_e32 v3, v3, v218
	v_sub_f32_e32 v4, v4, v218
	v_sub_f32_e32 v5, v5, v218
	v_sub_f32_e32 v6, v6, v218
	v_sub_f32_e32 v7, v7, v218
	v_sub_f32_e32 v8, v8, v218
	v_sub_f32_e32 v9, v9, v218
	v_sub_f32_e32 v10, v10, v218
	v_sub_f32_e32 v11, v11, v218
	v_sub_f32_e32 v12, v12, v218
	v_sub_f32_e32 v13, v13, v218
	v_sub_f32_e32 v14, v14, v218
	v_sub_f32_e32 v15, v15, v218
	v_sub_f32_e32 v16, v16, v218
	v_sub_f32_e32 v17, v17, v218
	v_sub_f32_e32 v222, v222, v218
	v_sub_f32_e32 v223, v223, v218
	v_sub_f32_e32 v224, v224, v218
	v_sub_f32_e32 v225, v225, v218
	v_sub_f32_e32 v226, v226, v218
	v_sub_f32_e32 v227, v227, v218
	v_sub_f32_e32 v228, v228, v218
	v_sub_f32_e32 v229, v229, v218
	v_sub_f32_e32 v230, v230, v218
	v_sub_f32_e32 v231, v231, v218
	v_sub_f32_e32 v232, v232, v218
	v_sub_f32_e32 v233, v233, v218
	v_sub_f32_e32 v234, v234, v218
	v_sub_f32_e32 v235, v235, v218
	v_sub_f32_e32 v236, v236, v218
	v_sub_f32_e32 v237, v237, v218
	v_pk_mul_f32 v[66:67], v[66:67], v[186:187] op_sel_hi:[1,0]
	v_pk_mul_f32 v[68:69], v[68:69], v[186:187] op_sel_hi:[1,0]
	v_pk_mul_f32 v[70:71], v[70:71], v[186:187] op_sel_hi:[1,0]
	v_pk_mul_f32 v[72:73], v[72:73], v[186:187] op_sel_hi:[1,0]
	v_pk_mul_f32 v[74:75], v[74:75], v[186:187] op_sel_hi:[1,0]
	v_pk_mul_f32 v[76:77], v[76:77], v[186:187] op_sel_hi:[1,0]
	v_pk_mul_f32 v[78:79], v[78:79], v[186:187] op_sel_hi:[1,0]
	v_pk_mul_f32 v[80:81], v[80:81], v[186:187] op_sel_hi:[1,0]
	v_pk_mul_f32 v[82:83], v[82:83], v[186:187] op_sel_hi:[1,0]
	v_pk_mul_f32 v[84:85], v[84:85], v[186:187] op_sel_hi:[1,0]
	v_pk_mul_f32 v[86:87], v[86:87], v[186:187] op_sel_hi:[1,0]
	v_pk_mul_f32 v[88:89], v[88:89], v[186:187] op_sel_hi:[1,0]
	v_pk_mul_f32 v[90:91], v[90:91], v[186:187] op_sel_hi:[1,0]
	v_pk_mul_f32 v[92:93], v[92:93], v[186:187] op_sel_hi:[1,0]
	v_pk_mul_f32 v[94:95], v[94:95], v[186:187] op_sel_hi:[1,0]
	v_pk_mul_f32 v[96:97], v[96:97], v[186:187] op_sel_hi:[1,0]
	v_mul_f32_e32 v202, v202, v186
.Lmla0_h0_noresc:
	v_exp_f32_e32 v18, v18
	v_exp_f32_e32 v19, v19
	v_exp_f32_e32 v20, v20
	v_exp_f32_e32 v21, v21
	v_exp_f32_e32 v22, v22
	v_exp_f32_e32 v23, v23
	v_exp_f32_e32 v24, v24
	v_exp_f32_e32 v25, v25
	v_add_f32_e32 v216, v18, v19
	v_add_f32_e32 v217, v20, v21
	v_exp_f32_e32 v26, v26
	v_exp_f32_e32 v27, v27
	v_exp_f32_e32 v28, v28
	v_exp_f32_e32 v29, v29
	v_add_f32_e32 v216, v216, v22
	v_add_f32_e32 v217, v217, v23
	s_waitcnt lgkmcnt(0)
	v_mfma_f32_32x32x16_bf16 v[50:65], v[34:37], v[130:133], v[222:237]
	ds_read_b64_tr_b16 v[178:179], v219 offset:0
	ds_read_b64_tr_b16 v[180:181], v219 offset:512
	v_add_f32_e32 v216, v216, v24
	v_add_f32_e32 v217, v217, v25
	v_exp_f32_e32 v30, v30
	v_mfma_f32_32x32x16_bf16 v[34:49], v[38:41], v[130:133], v[222:237]
	ds_read_b64_tr_b16 v[170:171], v219 offset:1024
	ds_read_b64_tr_b16 v[172:173], v219 offset:1536
	v_exp_f32_e32 v31, v31
	v_exp_f32_e32 v32, v32
	v_exp_f32_e32 v33, v33
	v_mfma_f32_32x32x16_bf16 v[50:65], v[98:101], v[134:137], v[50:65]
	ds_read_b64_tr_b16 v[162:163], v219 offset:2048
	ds_read_b64_tr_b16 v[164:165], v219 offset:2560
	v_add_f32_e32 v216, v216, v26
	v_add_f32_e32 v217, v217, v27
	v_add_f32_e32 v216, v216, v28
	v_mfma_f32_32x32x16_bf16 v[34:49], v[102:105], v[134:137], v[34:49]
	ds_read_b64_tr_b16 v[158:159], v219 offset:3072
	ds_read_b64_tr_b16 v[160:161], v219 offset:3584
	v_add_f32_e32 v217, v217, v29
	v_exp_f32_e32 v2, v2
	v_exp_f32_e32 v3, v3
	v_mfma_f32_32x32x16_bf16 v[50:65], v[106:109], v[138:141], v[50:65]
	ds_read_b64_tr_b16 v[182:183], v219 offset:4096
	ds_read_b64_tr_b16 v[184:185], v219 offset:4608
	v_exp_f32_e32 v4, v4
	v_exp_f32_e32 v5, v5
	v_add_f32_e32 v216, v216, v30
	v_mfma_f32_32x32x16_bf16 v[34:49], v[110:113], v[138:141], v[34:49]
	ds_read_b64_tr_b16 v[174:175], v219 offset:5120
	ds_read_b64_tr_b16 v[176:177], v219 offset:5632
	v_add_f32_e32 v217, v217, v31
	v_add_f32_e32 v216, v216, v32
	v_add_f32_e32 v217, v217, v33
	v_mfma_f32_32x32x16_bf16 v[50:65], v[114:117], v[142:145], v[50:65]
	ds_read_b64_tr_b16 v[166:167], v219 offset:6144
	ds_read_b64_tr_b16 v[168:169], v219 offset:6656
	v_exp_f32_e32 v6, v6
	v_exp_f32_e32 v7, v7
	v_exp_f32_e32 v8, v8
	v_mfma_f32_32x32x16_bf16 v[34:49], v[118:121], v[142:145], v[34:49]
	ds_read_b64_tr_b16 v[154:155], v219 offset:7168
	ds_read_b64_tr_b16 v[156:157], v219 offset:7680
	v_exp_f32_e32 v9, v9
	v_exp_f32_e32 v10, v10
	v_exp_f32_e32 v11, v11
	v_mfma_f32_32x32x16_bf16 v[50:65], v[122:125], v[146:149], v[50:65]
	s_cmp_eq_u32 s88, 0
	s_cbranch_scc1 .Lmla0_h0_stg_skip
	s_cmp_eq_u32 s92, 0
	s_cbranch_scc1 .Lmla0_h0_stg_full
	s_waitcnt vmcnt(2) lgkmcnt(0)
	s_barrier
	s_branch .Lmla0_h0_stg_skip

; template <bool ALIBI>
; __device__ __forceinline__ void attn_sv(const LAS unsigned char* kb, int vfo, f32x16& p0, f32x16& p1, float& m, float& l, f32x16& o0, f32x16& o1, int hi, int tq, int kpos0, float slope2, bool causal) {
;     ...
;     if (causal) {
; #pragma unroll
;         for (int r = 0; r < 16; ++r) { const int kv = krel + (r & 3) + 8 * (r >> 2); if (kv > 0) p0[r] = -INFINITY; if (kv + 32 > 0) p1[r] = -INFINITY; } }
;     float rm = fmaxf(p0[0], p1[0]);
; #pragma unroll
;     for (int r = 1; r < 16; ++r) rm = fmaxf(rm, fmaxf(p0[r], p1[r]));
;     rm = xhalf_max(rm);
;     const float mn = fmaxf(m, rm), alpha = __builtin_amdgcn_exp2f(m - mn);
;     ...
;     const u32x4 pw0 = (u32x4){pg8::cvt_pk_bf16(p0[0], p0[1]), pg8::cvt_pk_bf16(p0[2], p0[3]), pg8::cvt_pk_bf16(p0[4], p0[5]), pg8::cvt_pk_bf16(p0[6], p0[7])};
;     const u32x4 pw1 = (u32x4){pg8::cvt_pk_bf16(p0[8], p0[9]), pg8::cvt_pk_bf16(p0[10], p0[11]), pg8::cvt_pk_bf16(p0[12], p0[13]), pg8::cvt_pk_bf16(p0[14], p0[15])};
;     const u32x4 pw2 = (u32x4){pg8::cvt_pk_bf16(p1[0], p1[1]), pg8::cvt_pk_bf16(p1[2], p1[3]), pg8::cvt_pk_bf16(p1[4], p1[5]), pg8::cvt_pk_bf16(p1[6], p1[7])};
;     const u32x4 pw3 = (u32x4){pg8::cvt_pk_bf16(p1[8], p1[9]), pg8::cvt_pk_bf16(p1[10], p1[11]), pg8::cvt_pk_bf16(p1[12], p1[13]), pg8::cvt_pk_bf16(p1[14], p1[15])};
;     asm volatile("s_waitcnt lgkmcnt(0)" ::: "memory"); __builtin_amdgcn_sched_barrier(0);
;     ...
;     o0 = __builtin_amdgcn_mfma_f32_32x32x16_bf16(ATT_VF(0), __builtin_bit_cast(bf16x8, pw0), o0, 0, 0, 0);
;     o1 = __builtin_amdgcn_mfma_f32_32x32x16_bf16(ATT_VF(4), __builtin_bit_cast(bf16x8, pw0), o1, 0, 0, 0);
;     o0 = __builtin_amdgcn_mfma_f32_32x32x16_bf16(ATT_VF(1), __builtin_bit_cast(bf16x8, pw1), o0, 0, 0, 0);
;     o1 = __builtin_amdgcn_mfma_f32_32x32x16_bf16(ATT_VF(5), __builtin_bit_cast(bf16x8, pw1), o1, 0, 0, 0);
;     o0 = __builtin_amdgcn_mfma_f32_32x32x16_bf16(ATT_VF(2), __builtin_bit_cast(bf16x8, pw2), o0, 0, 0, 0);
;     o1 = __builtin_amdgcn_mfma_f32_32x32x16_bf16(ATT_VF(6), __builtin_bit_cast(bf16x8, pw2), o1, 0, 0, 0);
;     o0 = __builtin_amdgcn_mfma_f32_32x32x16_bf16(ATT_VF(3), __builtin_bit_cast(bf16x8, pw3), o0, 0, 0, 0);
;     o1 = __builtin_amdgcn_mfma_f32_32x32x16_bf16(ATT_VF(7), __builtin_bit_cast(bf16x8, pw3), o1, 0, 0, 0);
.Lmla0_h0_stg_skip:
	v_exp_f32_e32 v12, v12
	v_exp_f32_e32 v13, v13
	v_exp_f32_e32 v14, v14
	v_mfma_f32_32x32x16_bf16 v[34:49], v[126:129], v[146:149], v[34:49]
	v_exp_f32_e32 v15, v15
	v_exp_f32_e32 v16, v16
	v_exp_f32_e32 v17, v17
	v_mfma_f32_32x32x16_bf16 v[50:65], v[204:207], v[150:153], v[50:65]
	v_mfma_f32_32x32x16_bf16 v[34:49], v[208:211], v[150:153], v[34:49]
	s_cmp_lt_u32 s72, s77
	s_cbranch_scc1 .Lmla0_h0_nomask
	s_add_i32 s1, s72, 1
	s_nop 7
	s_nop 3
	v_lshl_add_u32 v220, s1, 6, v201
	v_sub_u32_e32 v220, 0, v220
	v_cmp_gt_i32_e64 s[8:9], 0, v220
	v_cmp_gt_i32_e64 s[10:11], 1, v220
	v_cmp_gt_i32_e64 s[12:13], 2, v220
	v_cmp_gt_i32_e64 s[14:15], 3, v220
	v_cmp_gt_i32_e64 s[16:17], 8, v220
	v_cmp_gt_i32_e64 s[18:19], 9, v220
	v_cmp_gt_i32_e64 s[20:21], 10, v220
	v_cmp_gt_i32_e64 s[22:23], 11, v220
	v_cndmask_b32_e64 v50, v50, v1, s[8:9]
	v_cndmask_b32_e64 v51, v51, v1, s[10:11]
	v_cndmask_b32_e64 v52, v52, v1, s[12:13]
	v_cndmask_b32_e64 v53, v53, v1, s[14:15]
	v_cndmask_b32_e64 v54, v54, v1, s[16:17]
	v_cndmask_b32_e64 v55, v55, v1, s[18:19]
	v_cndmask_b32_e64 v56, v56, v1, s[20:21]
	v_cndmask_b32_e64 v57, v57, v1, s[22:23]
	v_cmp_gt_i32_e64 s[8:9], 16, v220
	v_cmp_gt_i32_e64 s[10:11], 17, v220
	v_cmp_gt_i32_e64 s[12:13], 18, v220
	v_cmp_gt_i32_e64 s[14:15], 19, v220
	v_cmp_gt_i32_e64 s[16:17], 24, v220
	v_cmp_gt_i32_e64 s[18:19], 25, v220
	v_cmp_gt_i32_e64 s[20:21], 26, v220
	v_cmp_gt_i32_e64 s[22:23], 27, v220
	v_cndmask_b32_e64 v58, v58, v1, s[8:9]
	v_cndmask_b32_e64 v59, v59, v1, s[10:11]
	v_cndmask_b32_e64 v60, v60, v1, s[12:13]
	v_cndmask_b32_e64 v61, v61, v1, s[14:15]
	v_cndmask_b32_e64 v62, v62, v1, s[16:17]
	v_cndmask_b32_e64 v63, v63, v1, s[18:19]
	v_cndmask_b32_e64 v64, v64, v1, s[20:21]
	v_cndmask_b32_e64 v65, v65, v1, s[22:23]
	v_cmp_gt_i32_e64 s[8:9], 32, v220
	v_cmp_gt_i32_e64 s[10:11], 33, v220
	v_cmp_gt_i32_e64 s[12:13], 34, v220
	v_cmp_gt_i32_e64 s[14:15], 35, v220
	v_cmp_gt_i32_e64 s[16:17], 40, v220
	v_cmp_gt_i32_e64 s[18:19], 41, v220
	v_cmp_gt_i32_e64 s[20:21], 42, v220
	v_cmp_gt_i32_e64 s[22:23], 43, v220
	v_cndmask_b32_e64 v34, v34, v1, s[8:9]
	v_cndmask_b32_e64 v35, v35, v1, s[10:11]
	v_cndmask_b32_e64 v36, v36, v1, s[12:13]
	v_cndmask_b32_e64 v37, v37, v1, s[14:15]
	v_cndmask_b32_e64 v38, v38, v1, s[16:17]
	v_cndmask_b32_e64 v39, v39, v1, s[18:19]
	v_cndmask_b32_e64 v40, v40, v1, s[20:21]
	v_cndmask_b32_e64 v41, v41, v1, s[22:23]
	v_cmp_gt_i32_e64 s[8:9], 48, v220
	v_cmp_gt_i32_e64 s[10:11], 49, v220
	v_cmp_gt_i32_e64 s[12:13], 50, v220
	v_cmp_gt_i32_e64 s[14:15], 51, v220
	v_cmp_gt_i32_e64 s[16:17], 56, v220
	v_cmp_gt_i32_e64 s[18:19], 57, v220
	v_cmp_gt_i32_e64 s[20:21], 58, v220
	v_cmp_gt_i32_e64 s[22:23], 59, v220
	v_cndmask_b32_e64 v42, v42, v1, s[8:9]
	v_cndmask_b32_e64 v43, v43, v1, s[10:11]
	v_cndmask_b32_e64 v44, v44, v1, s[12:13]
	v_cndmask_b32_e64 v45, v45, v1, s[14:15]
	v_cndmask_b32_e64 v46, v46, v1, s[16:17]
	v_cndmask_b32_e64 v47, v47, v1, s[18:19]
	v_cndmask_b32_e64 v48, v48, v1, s[20:21]
	v_cndmask_b32_e64 v49, v49, v1, s[22:23]
.Lmla0_h0_nomask:
	s_nop 0
	v_cvt_pk_bf16_f32 v18, v18, v19
	v_cvt_pk_bf16_f32 v19, v20, v21
	v_cvt_pk_bf16_f32 v20, v22, v23
	v_cvt_pk_bf16_f32 v21, v24, v25
	v_add_f32_e32 v216, v216, v2
	v_add_f32_e32 v217, v217, v3
	s_waitcnt lgkmcnt(0)
	v_mfma_f32_32x32x16_bf16 v[66:81], v[178:181], v[18:21], v[66:81]
	v_add_f32_e32 v216, v216, v4
	v_add_f32_e32 v217, v217, v5
	v_cvt_pk_bf16_f32 v22, v26, v27
	v_cvt_pk_bf16_f32 v23, v28, v29
	v_cvt_pk_bf16_f32 v24, v30, v31
	v_cvt_pk_bf16_f32 v25, v32, v33
	v_mfma_f32_32x32x16_bf16 v[82:97], v[182:185], v[18:21], v[82:97]
	v_add_f32_e32 v216, v216, v6
	v_add_f32_e32 v217, v217, v7
	v_add_f32_e32 v216, v216, v8
	v_add_f32_e32 v217, v217, v9
	v_max3_f32 v218, v34, v35, v36
	v_max3_f32 v219, v50, v51, v52
	v_max3_f32 v218, v218, v37, v38
	v_max3_f32 v219, v219, v53, v54
	v_mfma_f32_32x32x16_bf16 v[66:81], v[170:173], v[22:25], v[66:81]
	v_cvt_pk_bf16_f32 v26, v2, v3
	v_cvt_pk_bf16_f32 v27, v4, v5
	v_cvt_pk_bf16_f32 v28, v6, v7
	v_cvt_pk_bf16_f32 v29, v8, v9
	v_max3_f32 v218, v218, v39, v40
	v_max3_f32 v219, v219, v55, v56
	v_max3_f32 v218, v218, v41, v42
	v_max3_f32 v219, v219, v57, v58
	v_mfma_f32_32x32x16_bf16 v[82:97], v[174:177], v[22:25], v[82:97]
	v_add_f32_e32 v216, v216, v10
	v_add_f32_e32 v217, v217, v11
	v_add_f32_e32 v216, v216, v12
	v_add_f32_e32 v217, v217, v13
	v_max3_f32 v218, v218, v43, v44
	v_max3_f32 v219, v219, v59, v60
	v_max3_f32 v218, v218, v45, v46
	v_max3_f32 v219, v219, v61, v62
	v_mfma_f32_32x32x16_bf16 v[66:81], v[162:165], v[26:29], v[66:81]
	v_add_f32_e32 v216, v216, v14
	v_add_f32_e32 v217, v217, v15
	v_add_f32_e32 v216, v216, v16
	v_add_f32_e32 v217, v217, v17
	v_max3_f32 v218, v218, v47, v48
	v_max3_f32 v219, v219, v63, v64
	v_max3_f32 v218, v218, v49, v219
	v_max_f32_e32 v218, v218, v65
	v_mfma_f32_32x32x16_bf16 v[82:97], v[166:169], v[26:29], v[82:97]
	v_cvt_pk_bf16_f32 v30, v10, v11
	v_cvt_pk_bf16_f32 v31, v12, v13
	v_cvt_pk_bf16_f32 v32, v14, v15
	v_cvt_pk_bf16_f32 v33, v16, v17
	v_mov_b32_e32 v219, v218
	v_add_f32_e32 v216, v216, v217
	v_add_f32_e32 v202, v202, v216
	v_mfma_f32_32x32x16_bf16 v[66:81], v[158:161], v[30:33], v[66:81]
	v_permlane32_swap_b32_e32 v218, v219
	v_max_f32_e32 v203, v218, v219
	s_nop 0
	v_cmp_lt_f32_e64 s[94:95], 4.0, v203
	v_mfma_f32_32x32x16_bf16 v[82:97], v[154:157], v[30:33], v[82:97]
	s_cmp_lg_u32 s88, 0
	s_cbranch_scc1 .Lmla0_h0_nobar
	s_cmp_eq_u32 s92, 0
	s_cbranch_scc1 .Lmla0_h0_full
	s_cmp_lg_u32 s88, 0
	s_cbranch_scc1 .Lmla0_h0_w2
	s_waitcnt vmcnt(3)
	s_branch .Lmla0_h0_bar

; #define LAS __attribute__((address_space(3)))
; #define ATT_ISSUE(t, bo) do { \
;         for (int c_ = wid; c_ < NCH; c_ += 8) __builtin_amdgcn_global_load_lds((const unsigned*)(ksrc + (size_t)(t) * 64 * ldk + c_ * 8), (LAS unsigned*)(lds + (bo) + c_ * 1024), 16, 0, 0); \
;         __builtin_amdgcn_global_load_lds((const unsigned*)(vsrc + (size_t)(t) * 64 * ldv), (LAS unsigned*)(lds + (bo) + KBYTES + wid * 1024), 16, 0, 0); } while (0)
; #define ATT_BAR() asm volatile("s_waitcnt vmcnt(0) lgkmcnt(0)\n\ts_barrier" ::: "memory")
; #define ATT_BARN() do { if (NCH > 8 && wid < NCH - 8) asm volatile("s_waitcnt vmcnt(3) lgkmcnt(0)\n\ts_barrier" ::: "memory"); else asm volatile("s_waitcnt vmcnt(2) lgkmcnt(0)\n\ts_barrier" ::: "memory"); } while (0)
; #define ATT_ROT() do { bi = __builtin_amdgcn_readfirstlane((bi + 1) & 3); } while (0)
; template <int DQK>
; __device__ __forceinline__ void attn_qk(const LAS unsigned char* kb, int kfo, const bf16x8 (&qf)[DQK / 16], f32x16& p0, f32x16& p1) {
;     ...
;     bf16x8 ka[ND0], kc[ND0];
; #pragma unroll
;     for (int d0 = 0; d0 < ND0; ++d0) { ka[d0] = *(const LAS bf16x8*)(kb + kfo + d0 * 2048); kc[d0] = *(const LAS bf16x8*)(kb + kfo + d0 * 2048 + 512); }
; template <int DQK, bool MOBA_OWN>
; __device__ __forceinline__ void attn_unit(LAS unsigned char* lds, int b, int h, int qb, const bf16_t* Qp, int ldq, const bf16_t* Kp, int ldk, const bf16_t* Vp, int ldv, bf16_t* Op, int ldo, const bf16_t* PO, const f32x2* PML) {
;     ...
;     for (int t = T0; t < T1; t += 2) {
;         const bool i1 = t + 3 < T1, i2 = t + 4 < T1;
;         if (i1) ATT_ISSUE(t + 3, b3);
;         attn_qk<DQK>(lds + b1, kfo, qf, pB0, pB1);
;         attn_sv<MOBA_OWN>(lds + b0, vfo, pA0, pA1, m, l, o0, o1, hi, tq, 64 * t, slope2, t >= T1 - 4);
;         if (i1) ATT_BARN(); else ATT_BAR();
;         ATT_ROT();
;         if (i2) ATT_ISSUE(t + 4, b3);
;         if (t + 2 < T1) attn_qk<DQK>(lds + b1, kfo, qf, pA0, pA1);
.Lmla0_h0_nobar:
	s_add_i32 s6, s6, 1
	s_and_b32 s6, s6, 3
	s_add_i32 s0, s72, 4
	s_cmp_lt_u32 s0, s78
	s_cselect_b32 s92, 1, 0
	s_add_i32 s1, s72, 2
	s_cmp_lt_u32 s1, s78
	s_cselect_b32 s93, 1, 0
	s_cmp_eq_u32 s93, 0
	s_cbranch_scc1 .Lmla0_h1_nokread
	s_add_i32 s4, s6, 1
	s_and_b32 s79, s4, 3
	s_mul_i32 s4, s79, 0x5000
	v_add_u32_e32 v218, s4, v199
	ds_read_b128 v[2:5], v218
	ds_read_b128 v[6:9], v218 offset:512
	ds_read_b128 v[98:101], v218 offset:2048
	ds_read_b128 v[102:105], v218 offset:2560
	ds_read_b128 v[106:109], v218 offset:4096
	ds_read_b128 v[110:113], v218 offset:4608
	ds_read_b128 v[114:117], v218 offset:6144
	ds_read_b128 v[118:121], v218 offset:6656
	ds_read_b128 v[122:125], v218 offset:8192
	ds_read_b128 v[126:129], v218 offset:8704
	ds_read_b128 v[204:207], v218 offset:10240
	ds_read_b128 v[208:211], v218 offset:10752

; template <int DQK>
; __device__ __forceinline__ void attn_qk(const LAS unsigned char* kb, int kfo, const bf16x8 (&qf)[DQK / 16], f32x16& p0, f32x16& p1) {
;     constexpr int ND0 = DQK / 16;
;     bf16x8 ka[ND0], kc[ND0];
; #pragma unroll
;     for (int d0 = 0; d0 < ND0; ++d0) { ka[d0] = *(const LAS bf16x8*)(kb + kfo + d0 * 2048); kc[d0] = *(const LAS bf16x8*)(kb + kfo + d0 * 2048 + 512); }
;     __builtin_amdgcn_sched_barrier(0);
; #pragma unroll
;     for (int r = 0; r < 16; ++r) { p0[r] = 0.f; p1[r] = 0.f; }
; #pragma unroll
;     for (int d0 = 0; d0 < ND0; ++d0) {
;         p0 = __builtin_amdgcn_mfma_f32_32x32x16_bf16(ka[d0], qf[d0], p0, 0, 0, 0);
;         p1 = __builtin_amdgcn_mfma_f32_32x32x16_bf16(kc[d0], qf[d0], p1, 0, 0, 0);
;     }
; }
; template <bool ALIBI>
; __device__ __forceinline__ void attn_sv(const LAS unsigned char* kb, int vfo, f32x16& p0, f32x16& p1, float& m, float& l, f32x16& o0, f32x16& o1, int hi, int tq, int kpos0, float slope2, bool causal) {
;     s16x4 vlo[8], vhi[8];
;     { const unsigned va = (unsigned)(uintptr_t)(kb + vfo);
; #pragma unroll
;       for (int i = 0; i < 8; ++i) {
;         asm volatile("ds_read_b64_tr_b16 %0, %1 offset:%c2" : "=&v"(vlo[i]) : "v"(va), "i"((i >> 2) * 4096 + (i & 3) * 1024) : "memory");
;         asm volatile("ds_read_b64_tr_b16 %0, %1 offset:%c2" : "=&v"(vhi[i]) : "v"(va), "i"((i >> 2) * 4096 + (i & 3) * 1024 + 512) : "memory"); } }
;     const int krel = kpos0 + 4 * hi - tq;
;     if (ALIBI) { const float bb = slope2 * (float)krel;
; #pragma unroll
;         for (int r = 0; r < 16; ++r) { const float c = (float)((r & 3) + 8 * (r >> 2)); p0[r] += fmaf(slope2, c, bb); p1[r] += fmaf(slope2, c + 32.f, bb); } }
;     if (causal) {
; #pragma unroll
;         for (int r = 0; r < 16; ++r) { const int kv = krel + (r & 3) + 8 * (r >> 2); if (kv > 0) p0[r] = -INFINITY; if (kv + 32 > 0) p1[r] = -INFINITY; } }
;     float rm = fmaxf(p0[0], p1[0]);
; #pragma unroll
;     for (int r = 1; r < 16; ++r) rm = fmaxf(rm, fmaxf(p0[r], p1[r]));
;     rm = xhalf_max(rm);
;     const float mn = fmaxf(m, rm), alpha = __builtin_amdgcn_exp2f(m - mn);
;     m = mn;
;     float ls = 0.f;
; #pragma unroll
;     for (int r = 0; r < 16; ++r) { p0[r] = __builtin_amdgcn_exp2f(p0[r] - mn); p1[r] = __builtin_amdgcn_exp2f(p1[r] - mn); ls += p0[r] + p1[r]; }
;     l = l * alpha + ls;
; #pragma unroll
.Lmla0_h1_noiss:
	s_cmp_lg_u64 s[94:95], 0
	s_cbranch_scc0 .Lmla0_h1_noresc
	v_max_f32_e32 v218, 0, v203
	v_exp_f32_e64 v186, -v218
	v_sub_f32_e32 v50, v50, v218
	v_sub_f32_e32 v51, v51, v218
	v_sub_f32_e32 v52, v52, v218
	v_sub_f32_e32 v53, v53, v218
	v_sub_f32_e32 v54, v54, v218
	v_sub_f32_e32 v55, v55, v218
	v_sub_f32_e32 v56, v56, v218
	v_sub_f32_e32 v57, v57, v218
	v_sub_f32_e32 v58, v58, v218
	v_sub_f32_e32 v59, v59, v218
	v_sub_f32_e32 v60, v60, v218
	v_sub_f32_e32 v61, v61, v218
	v_sub_f32_e32 v62, v62, v218
	v_sub_f32_e32 v63, v63, v218
	v_sub_f32_e32 v64, v64, v218
	v_sub_f32_e32 v65, v65, v218
	v_sub_f32_e32 v34, v34, v218
	v_sub_f32_e32 v35, v35, v218
	v_sub_f32_e32 v36, v36, v218
	v_sub_f32_e32 v37, v37, v218
	v_sub_f32_e32 v38, v38, v218
	v_sub_f32_e32 v39, v39, v218
	v_sub_f32_e32 v40, v40, v218
	v_sub_f32_e32 v41, v41, v218
	v_sub_f32_e32 v42, v42, v218
	v_sub_f32_e32 v43, v43, v218
	v_sub_f32_e32 v44, v44, v218
	v_sub_f32_e32 v45, v45, v218
	v_sub_f32_e32 v46, v46, v218
	v_sub_f32_e32 v47, v47, v218
	v_sub_f32_e32 v48, v48, v218
	v_sub_f32_e32 v49, v49, v218
	v_sub_f32_e32 v222, v222, v218
	v_sub_f32_e32 v223, v223, v218
	v_sub_f32_e32 v224, v224, v218
	v_sub_f32_e32 v225, v225, v218
	v_sub_f32_e32 v226, v226, v218
	v_sub_f32_e32 v227, v227, v218
	v_sub_f32_e32 v228, v228, v218
	v_sub_f32_e32 v229, v229, v218
	v_sub_f32_e32 v230, v230, v218
	v_sub_f32_e32 v231, v231, v218
	v_sub_f32_e32 v232, v232, v218
	v_sub_f32_e32 v233, v233, v218
	v_sub_f32_e32 v234, v234, v218
	v_sub_f32_e32 v235, v235, v218
	v_sub_f32_e32 v236, v236, v218
	v_sub_f32_e32 v237, v237, v218
	v_pk_mul_f32 v[66:67], v[66:67], v[186:187] op_sel_hi:[1,0]
	v_pk_mul_f32 v[68:69], v[68:69], v[186:187] op_sel_hi:[1,0]
	v_pk_mul_f32 v[70:71], v[70:71], v[186:187] op_sel_hi:[1,0]
	v_pk_mul_f32 v[72:73], v[72:73], v[186:187] op_sel_hi:[1,0]
	v_pk_mul_f32 v[74:75], v[74:75], v[186:187] op_sel_hi:[1,0]
	v_pk_mul_f32 v[76:77], v[76:77], v[186:187] op_sel_hi:[1,0]
	v_pk_mul_f32 v[78:79], v[78:79], v[186:187] op_sel_hi:[1,0]
	v_pk_mul_f32 v[80:81], v[80:81], v[186:187] op_sel_hi:[1,0]
	v_pk_mul_f32 v[82:83], v[82:83], v[186:187] op_sel_hi:[1,0]
	v_pk_mul_f32 v[84:85], v[84:85], v[186:187] op_sel_hi:[1,0]
	v_pk_mul_f32 v[86:87], v[86:87], v[186:187] op_sel_hi:[1,0]
	v_pk_mul_f32 v[88:89], v[88:89], v[186:187] op_sel_hi:[1,0]
	v_pk_mul_f32 v[90:91], v[90:91], v[186:187] op_sel_hi:[1,0]
	v_pk_mul_f32 v[92:93], v[92:93], v[186:187] op_sel_hi:[1,0]
	v_pk_mul_f32 v[94:95], v[94:95], v[186:187] op_sel_hi:[1,0]
	v_pk_mul_f32 v[96:97], v[96:97], v[186:187] op_sel_hi:[1,0]
	v_mul_f32_e32 v202, v202, v186
.Lmla0_h1_noresc:
	v_exp_f32_e32 v50, v50
	v_exp_f32_e32 v51, v51
	v_exp_f32_e32 v52, v52
	v_exp_f32_e32 v53, v53
	v_exp_f32_e32 v54, v54
	v_exp_f32_e32 v55, v55
	v_exp_f32_e32 v56, v56
	v_exp_f32_e32 v57, v57
	v_add_f32_e32 v216, v50, v51
	v_add_f32_e32 v217, v52, v53
	v_exp_f32_e32 v58, v58
	v_exp_f32_e32 v59, v59
	v_exp_f32_e32 v60, v60
	v_exp_f32_e32 v61, v61
	v_add_f32_e32 v216, v216, v54
	v_add_f32_e32 v217, v217, v55
	s_cmp_eq_u32 s93, 0
	s_cbranch_scc1 .Lmla0_h1_noqk
	s_waitcnt lgkmcnt(0)
	v_mfma_f32_32x32x16_bf16 v[18:33], v[2:5], v[130:133], v[222:237]
	ds_read_b64_tr_b16 v[178:179], v219 offset:0
	ds_read_b64_tr_b16 v[180:181], v219 offset:512
	v_add_f32_e32 v216, v216, v56
	v_add_f32_e32 v217, v217, v57
	v_exp_f32_e32 v62, v62
	v_mfma_f32_32x32x16_bf16 v[2:17], v[6:9], v[130:133], v[222:237]
	ds_read_b64_tr_b16 v[170:171], v219 offset:1024
	ds_read_b64_tr_b16 v[172:173], v219 offset:1536
	v_exp_f32_e32 v63, v63
	v_exp_f32_e32 v64, v64
	v_exp_f32_e32 v65, v65
	v_mfma_f32_32x32x16_bf16 v[18:33], v[98:101], v[134:137], v[18:33]
	ds_read_b64_tr_b16 v[162:163], v219 offset:2048
	ds_read_b64_tr_b16 v[164:165], v219 offset:2560
	v_add_f32_e32 v216, v216, v58
	v_add_f32_e32 v217, v217, v59
	v_add_f32_e32 v216, v216, v60
	v_mfma_f32_32x32x16_bf16 v[2:17], v[102:105], v[134:137], v[2:17]
	ds_read_b64_tr_b16 v[158:159], v219 offset:3072
	ds_read_b64_tr_b16 v[160:161], v219 offset:3584
	v_add_f32_e32 v217, v217, v61
	v_exp_f32_e32 v34, v34
	v_exp_f32_e32 v35, v35
	v_mfma_f32_32x32x16_bf16 v[18:33], v[106:109], v[138:141], v[18:33]
	ds_read_b64_tr_b16 v[182:183], v219 offset:4096
	ds_read_b64_tr_b16 v[184:185], v219 offset:4608
	v_exp_f32_e32 v36, v36
	v_exp_f32_e32 v37, v37
	v_add_f32_e32 v216, v216, v62
	v_mfma_f32_32x32x16_bf16 v[2:17], v[110:113], v[138:141], v[2:17]
	ds_read_b64_tr_b16 v[174:175], v219 offset:5120
	ds_read_b64_tr_b16 v[176:177], v219 offset:5632
	v_add_f32_e32 v217, v217, v63
	v_add_f32_e32 v216, v216, v64
	v_add_f32_e32 v217, v217, v65
	v_mfma_f32_32x32x16_bf16 v[18:33], v[114:117], v[142:145], v[18:33]
	ds_read_b64_tr_b16 v[166:167], v219 offset:6144
	ds_read_b64_tr_b16 v[168:169], v219 offset:6656
	v_exp_f32_e32 v38, v38
	v_exp_f32_e32 v39, v39
	v_exp_f32_e32 v40, v40
	v_mfma_f32_32x32x16_bf16 v[2:17], v[118:121], v[142:145], v[2:17]
	ds_read_b64_tr_b16 v[154:155], v219 offset:7168
	ds_read_b64_tr_b16 v[156:157], v219 offset:7680
	v_exp_f32_e32 v41, v41
	v_exp_f32_e32 v42, v42
	v_exp_f32_e32 v43, v43
	v_mfma_f32_32x32x16_bf16 v[18:33], v[122:125], v[146:149], v[18:33]
	s_cmp_eq_u32 s88, 0
	s_cbranch_scc1 .Lmla0_h1_stg_skip
	s_cmp_eq_u32 s92, 0
	s_cbranch_scc1 .Lmla0_h1_stg_full
	s_waitcnt vmcnt(2) lgkmcnt(0)
	s_barrier
	s_branch .Lmla0_h1_stg_skip

; #define LAS __attribute__((address_space(3)))
; template <int DQK>
; __device__ __forceinline__ void attn_qk(const LAS unsigned char* kb, int kfo, const bf16x8 (&qf)[DQK / 16], f32x16& p0, f32x16& p1) {
;     ...
;     for (int d0 = 0; d0 < ND0; ++d0) {
;         p0 = __builtin_amdgcn_mfma_f32_32x32x16_bf16(ka[d0], qf[d0], p0, 0, 0, 0);
;         p1 = __builtin_amdgcn_mfma_f32_32x32x16_bf16(kc[d0], qf[d0], p1, 0, 0, 0);
;     }
; }
; template <bool ALIBI>
; __device__ __forceinline__ void attn_sv(const LAS unsigned char* kb, int vfo, f32x16& p0, f32x16& p1, float& m, float& l, f32x16& o0, f32x16& o1, int hi, int tq, int kpos0, float slope2, bool causal) {
;     s16x4 vlo[8], vhi[8];
;     { const unsigned va = (unsigned)(uintptr_t)(kb + vfo);
; #pragma unroll
;       for (int i = 0; i < 8; ++i) {
;         asm volatile("ds_read_b64_tr_b16 %0, %1 offset:%c2" : "=&v"(vlo[i]) : "v"(va), "i"((i >> 2) * 4096 + (i & 3) * 1024) : "memory");
;         asm volatile("ds_read_b64_tr_b16 %0, %1 offset:%c2" : "=&v"(vhi[i]) : "v"(va), "i"((i >> 2) * 4096 + (i & 3) * 1024 + 512) : "memory"); } }
;     const int krel = kpos0 + 4 * hi - tq;
;     if (ALIBI) { const float bb = slope2 * (float)krel;
; #pragma unroll
;         for (int r = 0; r < 16; ++r) { const float c = (float)((r & 3) + 8 * (r >> 2)); p0[r] += fmaf(slope2, c, bb); p1[r] += fmaf(slope2, c + 32.f, bb); } }
;     if (causal) {
; #pragma unroll
;         for (int r = 0; r < 16; ++r) { const int kv = krel + (r & 3) + 8 * (r >> 2); if (kv > 0) p0[r] = -INFINITY; if (kv + 32 > 0) p1[r] = -INFINITY; } }
.Lmla0_h1_stg_skip:
	v_exp_f32_e32 v44, v44
	v_exp_f32_e32 v45, v45
	v_exp_f32_e32 v46, v46
	v_mfma_f32_32x32x16_bf16 v[2:17], v[126:129], v[146:149], v[2:17]
	v_exp_f32_e32 v47, v47
	v_exp_f32_e32 v48, v48
	v_exp_f32_e32 v49, v49
	v_mfma_f32_32x32x16_bf16 v[18:33], v[204:207], v[150:153], v[18:33]
	v_mfma_f32_32x32x16_bf16 v[2:17], v[208:211], v[150:153], v[2:17]
	s_add_i32 s1, s72, 2
	s_cmp_lt_u32 s1, s77
	s_cbranch_scc1 .Lmla0_h1_nomask
	s_nop 7
	s_nop 3
	v_lshl_add_u32 v220, s1, 6, v201
	v_sub_u32_e32 v220, 0, v220
	v_cmp_gt_i32_e64 s[8:9], 0, v220
	v_cmp_gt_i32_e64 s[10:11], 1, v220
	v_cmp_gt_i32_e64 s[12:13], 2, v220
	v_cmp_gt_i32_e64 s[14:15], 3, v220
	v_cmp_gt_i32_e64 s[16:17], 8, v220
	v_cmp_gt_i32_e64 s[18:19], 9, v220
	v_cmp_gt_i32_e64 s[20:21], 10, v220
	v_cmp_gt_i32_e64 s[22:23], 11, v220
	v_cndmask_b32_e64 v18, v18, v1, s[8:9]
	v_cndmask_b32_e64 v19, v19, v1, s[10:11]
	v_cndmask_b32_e64 v20, v20, v1, s[12:13]
	v_cndmask_b32_e64 v21, v21, v1, s[14:15]
	v_cndmask_b32_e64 v22, v22, v1, s[16:17]
	v_cndmask_b32_e64 v23, v23, v1, s[18:19]
	v_cndmask_b32_e64 v24, v24, v1, s[20:21]
	v_cndmask_b32_e64 v25, v25, v1, s[22:23]
	v_cmp_gt_i32_e64 s[8:9], 16, v220
	v_cmp_gt_i32_e64 s[10:11], 17, v220
	v_cmp_gt_i32_e64 s[12:13], 18, v220
	v_cmp_gt_i32_e64 s[14:15], 19, v220
	v_cmp_gt_i32_e64 s[16:17], 24, v220
	v_cmp_gt_i32_e64 s[18:19], 25, v220
	v_cmp_gt_i32_e64 s[20:21], 26, v220
	v_cmp_gt_i32_e64 s[22:23], 27, v220
	v_cndmask_b32_e64 v26, v26, v1, s[8:9]
	v_cndmask_b32_e64 v27, v27, v1, s[10:11]
	v_cndmask_b32_e64 v28, v28, v1, s[12:13]
	v_cndmask_b32_e64 v29, v29, v1, s[14:15]
	v_cndmask_b32_e64 v30, v30, v1, s[16:17]
	v_cndmask_b32_e64 v31, v31, v1, s[18:19]
	v_cndmask_b32_e64 v32, v32, v1, s[20:21]
	v_cndmask_b32_e64 v33, v33, v1, s[22:23]
	v_cmp_gt_i32_e64 s[8:9], 32, v220
	v_cmp_gt_i32_e64 s[10:11], 33, v220
	v_cmp_gt_i32_e64 s[12:13], 34, v220
	v_cmp_gt_i32_e64 s[14:15], 35, v220
	v_cmp_gt_i32_e64 s[16:17], 40, v220
	v_cmp_gt_i32_e64 s[18:19], 41, v220
	v_cmp_gt_i32_e64 s[20:21], 42, v220
	v_cmp_gt_i32_e64 s[22:23], 43, v220
	v_cndmask_b32_e64 v2, v2, v1, s[8:9]
	v_cndmask_b32_e64 v3, v3, v1, s[10:11]
	v_cndmask_b32_e64 v4, v4, v1, s[12:13]
	v_cndmask_b32_e64 v5, v5, v1, s[14:15]
	v_cndmask_b32_e64 v6, v6, v1, s[16:17]
	v_cndmask_b32_e64 v7, v7, v1, s[18:19]
	v_cndmask_b32_e64 v8, v8, v1, s[20:21]
	v_cndmask_b32_e64 v9, v9, v1, s[22:23]
	v_cmp_gt_i32_e64 s[8:9], 48, v220
	v_cmp_gt_i32_e64 s[10:11], 49, v220
	v_cmp_gt_i32_e64 s[12:13], 50, v220
	v_cmp_gt_i32_e64 s[14:15], 51, v220
	v_cmp_gt_i32_e64 s[16:17], 56, v220
	v_cmp_gt_i32_e64 s[18:19], 57, v220
	v_cmp_gt_i32_e64 s[20:21], 58, v220
	v_cmp_gt_i32_e64 s[22:23], 59, v220
	v_cndmask_b32_e64 v10, v10, v1, s[8:9]
	v_cndmask_b32_e64 v11, v11, v1, s[10:11]
	v_cndmask_b32_e64 v12, v12, v1, s[12:13]
	v_cndmask_b32_e64 v13, v13, v1, s[14:15]
	v_cndmask_b32_e64 v14, v14, v1, s[16:17]
	v_cndmask_b32_e64 v15, v15, v1, s[18:19]
	v_cndmask_b32_e64 v16, v16, v1, s[20:21]
	v_cndmask_b32_e64 v17, v17, v1, s[22:23]

; template <bool ALIBI>
; __device__ __forceinline__ void attn_sv(const LAS unsigned char* kb, int vfo, f32x16& p0, f32x16& p1, float& m, float& l, f32x16& o0, f32x16& o1, int hi, int tq, int kpos0, float slope2, bool causal) {
;     ...
;     float rm = fmaxf(p0[0], p1[0]);
; #pragma unroll
;     for (int r = 1; r < 16; ++r) rm = fmaxf(rm, fmaxf(p0[r], p1[r]));
;     rm = xhalf_max(rm);
;     const float mn = fmaxf(m, rm), alpha = __builtin_amdgcn_exp2f(m - mn);
;     m = mn;
;     float ls = 0.f;
; #pragma unroll
;     for (int r = 0; r < 16; ++r) { p0[r] = __builtin_amdgcn_exp2f(p0[r] - mn); p1[r] = __builtin_amdgcn_exp2f(p1[r] - mn); ls += p0[r] + p1[r]; }
;     l = l * alpha + ls;
; #pragma unroll
;     for (int r = 0; r < 16; ++r) { o0[r] *= alpha; o1[r] *= alpha; }
;     const u32x4 pw0 = (u32x4){pg8::cvt_pk_bf16(p0[0], p0[1]), pg8::cvt_pk_bf16(p0[2], p0[3]), pg8::cvt_pk_bf16(p0[4], p0[5]), pg8::cvt_pk_bf16(p0[6], p0[7])};
;     const u32x4 pw1 = (u32x4){pg8::cvt_pk_bf16(p0[8], p0[9]), pg8::cvt_pk_bf16(p0[10], p0[11]), pg8::cvt_pk_bf16(p0[12], p0[13]), pg8::cvt_pk_bf16(p0[14], p0[15])};
;     const u32x4 pw2 = (u32x4){pg8::cvt_pk_bf16(p1[0], p1[1]), pg8::cvt_pk_bf16(p1[2], p1[3]), pg8::cvt_pk_bf16(p1[4], p1[5]), pg8::cvt_pk_bf16(p1[6], p1[7])};
;     const u32x4 pw3 = (u32x4){pg8::cvt_pk_bf16(p1[8], p1[9]), pg8::cvt_pk_bf16(p1[10], p1[11]), pg8::cvt_pk_bf16(p1[12], p1[13]), pg8::cvt_pk_bf16(p1[14], p1[15])};
;     asm volatile("s_waitcnt lgkmcnt(0)" ::: "memory"); __builtin_amdgcn_sched_barrier(0);
;     ...
;     o0 = __builtin_amdgcn_mfma_f32_32x32x16_bf16(ATT_VF(0), __builtin_bit_cast(bf16x8, pw0), o0, 0, 0, 0);
;     o1 = __builtin_amdgcn_mfma_f32_32x32x16_bf16(ATT_VF(4), __builtin_bit_cast(bf16x8, pw0), o1, 0, 0, 0);
;     o0 = __builtin_amdgcn_mfma_f32_32x32x16_bf16(ATT_VF(1), __builtin_bit_cast(bf16x8, pw1), o0, 0, 0, 0);
;     o1 = __builtin_amdgcn_mfma_f32_32x32x16_bf16(ATT_VF(5), __builtin_bit_cast(bf16x8, pw1), o1, 0, 0, 0);
;     o0 = __builtin_amdgcn_mfma_f32_32x32x16_bf16(ATT_VF(2), __builtin_bit_cast(bf16x8, pw2), o0, 0, 0, 0);
;     o1 = __builtin_amdgcn_mfma_f32_32x32x16_bf16(ATT_VF(6), __builtin_bit_cast(bf16x8, pw2), o1, 0, 0, 0);
;     o0 = __builtin_amdgcn_mfma_f32_32x32x16_bf16(ATT_VF(3), __builtin_bit_cast(bf16x8, pw3), o0, 0, 0, 0);
;     o1 = __builtin_amdgcn_mfma_f32_32x32x16_bf16(ATT_VF(7), __builtin_bit_cast(bf16x8, pw3), o1, 0, 0, 0);
.Lmla0_h1_noqk:
	ds_read_b64_tr_b16 v[178:179], v219 offset:0
	ds_read_b64_tr_b16 v[180:181], v219 offset:512
	ds_read_b64_tr_b16 v[170:171], v219 offset:1024
	ds_read_b64_tr_b16 v[172:173], v219 offset:1536
	ds_read_b64_tr_b16 v[162:163], v219 offset:2048
	ds_read_b64_tr_b16 v[164:165], v219 offset:2560
	ds_read_b64_tr_b16 v[158:159], v219 offset:3072
	ds_read_b64_tr_b16 v[160:161], v219 offset:3584
	ds_read_b64_tr_b16 v[182:183], v219 offset:4096
	ds_read_b64_tr_b16 v[184:185], v219 offset:4608
	ds_read_b64_tr_b16 v[174:175], v219 offset:5120
	ds_read_b64_tr_b16 v[176:177], v219 offset:5632
	ds_read_b64_tr_b16 v[166:167], v219 offset:6144
	ds_read_b64_tr_b16 v[168:169], v219 offset:6656
	ds_read_b64_tr_b16 v[154:155], v219 offset:7168
	ds_read_b64_tr_b16 v[156:157], v219 offset:7680
	s_cmp_eq_u32 s88, 0
	s_cbranch_scc1 .Lmla0_h1_stg_skip2
	s_waitcnt vmcnt(0) lgkmcnt(0)
	s_barrier
.Lmla0_h1_stg_skip2:
	v_add_f32_e32 v216, v216, v56
	v_add_f32_e32 v217, v217, v57
	v_exp_f32_e32 v62, v62
	v_exp_f32_e32 v63, v63
	v_exp_f32_e32 v64, v64
	v_exp_f32_e32 v65, v65
	v_add_f32_e32 v216, v216, v58
	v_add_f32_e32 v217, v217, v59
	v_add_f32_e32 v216, v216, v60
	v_add_f32_e32 v217, v217, v61
	v_exp_f32_e32 v34, v34
	v_exp_f32_e32 v35, v35
	v_exp_f32_e32 v36, v36
	v_exp_f32_e32 v37, v37
	v_add_f32_e32 v216, v216, v62
	v_add_f32_e32 v217, v217, v63
	v_add_f32_e32 v216, v216, v64
	v_add_f32_e32 v217, v217, v65
	v_exp_f32_e32 v38, v38
	v_exp_f32_e32 v39, v39
	v_exp_f32_e32 v40, v40
	v_exp_f32_e32 v41, v41
	v_exp_f32_e32 v42, v42
	v_exp_f32_e32 v43, v43
	v_exp_f32_e32 v44, v44
	v_exp_f32_e32 v45, v45
	v_exp_f32_e32 v46, v46
	v_exp_f32_e32 v47, v47
	v_exp_f32_e32 v48, v48
	v_exp_f32_e32 v49, v49
.Lmla0_h1_qkdone:
	s_nop 0
	v_cvt_pk_bf16_f32 v50, v50, v51
	v_cvt_pk_bf16_f32 v51, v52, v53
	v_cvt_pk_bf16_f32 v52, v54, v55
	v_cvt_pk_bf16_f32 v53, v56, v57
	v_add_f32_e32 v216, v216, v34
	v_add_f32_e32 v217, v217, v35
	s_waitcnt lgkmcnt(0)
	v_mfma_f32_32x32x16_bf16 v[66:81], v[178:181], v[50:53], v[66:81]
	v_add_f32_e32 v216, v216, v36
	v_add_f32_e32 v217, v217, v37
	v_cvt_pk_bf16_f32 v54, v58, v59
	v_cvt_pk_bf16_f32 v55, v60, v61
	v_cvt_pk_bf16_f32 v56, v62, v63
	v_cvt_pk_bf16_f32 v57, v64, v65
	v_mfma_f32_32x32x16_bf16 v[82:97], v[182:185], v[50:53], v[82:97]
	v_add_f32_e32 v216, v216, v38
	v_add_f32_e32 v217, v217, v39
	v_add_f32_e32 v216, v216, v40
	v_add_f32_e32 v217, v217, v41
	v_max3_f32 v218, v2, v3, v4
	v_max3_f32 v219, v18, v19, v20
	v_max3_f32 v218, v218, v5, v6
	v_max3_f32 v219, v219, v21, v22
	v_mfma_f32_32x32x16_bf16 v[66:81], v[170:173], v[54:57], v[66:81]
	v_cvt_pk_bf16_f32 v58, v34, v35
	v_cvt_pk_bf16_f32 v59, v36, v37
	v_cvt_pk_bf16_f32 v60, v38, v39
	v_cvt_pk_bf16_f32 v61, v40, v41
	v_max3_f32 v218, v218, v7, v8
	v_max3_f32 v219, v219, v23, v24
	v_max3_f32 v218, v218, v9, v10
	v_max3_f32 v219, v219, v25, v26
	v_mfma_f32_32x32x16_bf16 v[82:97], v[174:177], v[54:57], v[82:97]
	v_add_f32_e32 v216, v216, v42
	v_add_f32_e32 v217, v217, v43
	v_add_f32_e32 v216, v216, v44
	v_add_f32_e32 v217, v217, v45
	v_max3_f32 v218, v218, v11, v12
	v_max3_f32 v219, v219, v27, v28
	v_max3_f32 v218, v218, v13, v14
	v_max3_f32 v219, v219, v29, v30
	v_mfma_f32_32x32x16_bf16 v[66:81], v[162:165], v[58:61], v[66:81]
	v_add_f32_e32 v216, v216, v46
	v_add_f32_e32 v217, v217, v47
	v_add_f32_e32 v216, v216, v48
	v_add_f32_e32 v217, v217, v49
	v_max3_f32 v218, v218, v15, v16
	v_max3_f32 v219, v219, v31, v32
	v_max3_f32 v218, v218, v17, v219
	v_max_f32_e32 v218, v218, v33
	v_mfma_f32_32x32x16_bf16 v[82:97], v[166:169], v[58:61], v[82:97]
	v_cvt_pk_bf16_f32 v62, v42, v43
	v_cvt_pk_bf16_f32 v63, v44, v45
	v_cvt_pk_bf16_f32 v64, v46, v47
	v_cvt_pk_bf16_f32 v65, v48, v49
	v_mov_b32_e32 v219, v218
	v_add_f32_e32 v216, v216, v217
	v_add_f32_e32 v202, v202, v216
	v_mfma_f32_32x32x16_bf16 v[66:81], v[158:161], v[62:65], v[66:81]
	v_permlane32_swap_b32_e32 v218, v219
	v_max_f32_e32 v214, v218, v219
	s_nop 0
	v_cmp_lt_f32_e64 s[90:91], 4.0, v214
	v_mfma_f32_32x32x16_bf16 v[82:97], v[154:157], v[62:65], v[82:97]
	s_cmp_lg_u32 s88, 0
	s_cbranch_scc1 .Lmla0_h1_nobar
	s_cmp_eq_u32 s92, 0
	s_cbranch_scc1 .Lmla0_h1_full
	s_cmp_lg_u32 s88, 0
	s_cbranch_scc1 .Lmla0_h1_w2
	s_waitcnt vmcnt(3)
	s_branch .Lmla0_h1_bar

; #define ATT_ISSUE(t, bo) do { \
;         for (int c_ = wid; c_ < NCH; c_ += 8) __builtin_amdgcn_global_load_lds((const unsigned*)(ksrc + (size_t)(t) * 64 * ldk + c_ * 8), (LAS unsigned*)(lds + (bo) + c_ * 1024), 16, 0, 0); \
;         __builtin_amdgcn_global_load_lds((const unsigned*)(vsrc + (size_t)(t) * 64 * ldv), (LAS unsigned*)(lds + (bo) + KBYTES + wid * 1024), 16, 0, 0); } while (0)
; #define ATT_BAR() asm volatile("s_waitcnt vmcnt(0) lgkmcnt(0)\n\ts_barrier" ::: "memory")
; #define ATT_BARN() do { if (NCH > 8 && wid < NCH - 8) asm volatile("s_waitcnt vmcnt(3) lgkmcnt(0)\n\ts_barrier" ::: "memory"); else asm volatile("s_waitcnt vmcnt(2) lgkmcnt(0)\n\ts_barrier" ::: "memory"); } while (0)
; #define ATT_ROT() do { bi = __builtin_amdgcn_readfirstlane((bi + 1) & 3); } while (0)
; template <int DQK, bool MOBA_OWN>
; __device__ __forceinline__ void attn_unit(LAS unsigned char* lds, int b, int h, int qb, const bf16_t* Qp, int ldq, const bf16_t* Kp, int ldk, const bf16_t* Vp, int ldv, bf16_t* Op, int ldo, const bf16_t* PO, const f32x2* PML) {
;     ...
;         if (i1) ATT_BARN(); else ATT_BAR();
;         ATT_ROT();
;         if (i2) ATT_ISSUE(t + 4, b3);
;         if (t + 2 < T1) attn_qk<DQK>(lds + b1, kfo, qf, pA0, pA1);
;         attn_sv<MOBA_OWN>(lds + b0, vfo, pB0, pB1, m, l, o0, o1, hi, tq, 64 * (t + 1), slope2, t + 1 >= T1 - 4);
;         if (i2) ATT_BARN(); else ATT_BAR();
;         ATT_ROT();
;     }
.Lmla0_h1_nobar:
	s_add_i32 s6, s6, 1
	s_and_b32 s6, s6, 3
	v_lshl_add_u64 v[194:195], v[194:195], 0, s[66:67]
	v_lshl_add_u64 v[196:197], v[196:197], 0, s[66:67]
	s_add_i32 s72, s72, 2
	s_cmp_lt_u32 s72, s78
	s_cbranch_scc1 .Lmla0_loop
	s_branch .LBB0_760

; #define ATT_ISSUE(t, bo) do { \
;         for (int c_ = wid; c_ < NCH; c_ += 8) __builtin_amdgcn_global_load_lds((const unsigned*)(ksrc + (size_t)(t) * 64 * ldk + c_ * 8), (LAS unsigned*)(lds + (bo) + c_ * 1024), 16, 0, 0); \
;         __builtin_amdgcn_global_load_lds((const unsigned*)(vsrc + (size_t)(t) * 64 * ldv), (LAS unsigned*)(lds + (bo) + KBYTES + wid * 1024), 16, 0, 0); } while (0)
; #define ATT_BAR() asm volatile("s_waitcnt vmcnt(0) lgkmcnt(0)\n\ts_barrier" ::: "memory")
; #define ATT_BARN() do { if (NCH > 8 && wid < NCH - 8) asm volatile("s_waitcnt vmcnt(3) lgkmcnt(0)\n\ts_barrier" ::: "memory"); else asm volatile("s_waitcnt vmcnt(2) lgkmcnt(0)\n\ts_barrier" ::: "memory"); } while (0)
; #define ATT_ROT() do { bi = __builtin_amdgcn_readfirstlane((bi + 1) & 3); } while (0)
; template <int DQK, bool MOBA_OWN>
; __device__ __forceinline__ void attn_unit(LAS unsigned char* lds, int b, int h, int qb, const bf16_t* Qp, int ldq, const bf16_t* Kp, int ldk, const bf16_t* Vp, int ldv, bf16_t* Op, int ldo, const bf16_t* PO, const f32x2* PML) {
;     ...
;         if (i1) ATT_BARN(); else ATT_BAR();
;         ATT_ROT();
;         if (i2) ATT_ISSUE(t + 4, b3);
;         if (t + 2 < T1) attn_qk<DQK>(lds + b1, kfo, qf, pA0, pA1);
;         attn_sv<MOBA_OWN>(lds + b0, vfo, pB0, pB1, m, l, o0, o1, hi, tq, 64 * (t + 1), slope2, t + 1 >= T1 - 4);
;         if (i2) ATT_BARN(); else ATT_BAR();
;         ATT_ROT();
;     }
.Lmla1_h1_nobar:
	s_add_i32 s6, s6, 1
	s_and_b32 s6, s6, 3
	v_lshl_add_u64 v[194:195], v[194:195], 0, s[68:69]
	v_lshl_add_u64 v[196:197], v[196:197], 0, s[68:69]
	s_add_i32 s72, s72, 2
	s_cmp_lt_u32 s72, s78
	s_cbranch_scc1 .Lmla1_loop
	s_branch .LBB0_3219
